# attention tasks: static s_setprio 2 moved to waves 0-3 instead of waves 4-7 (opposite skew of the previous version)
# speedup vs baseline: 1.0048x; 1.0037x over previous
; __global__ void __launch_bounds__(NWAVES * 64, 2) hybrid_fwd(Args args) {
;     ...
;                     const int n = g < 128 ? 1 : 3, w = g - 128;
;                     for (int i = 0; i < n; ++i) {
;                         const int task = g < 128 ? t12(g) : (i < 2 ? t12(128 + 2 * w + i) : (w < 64 ? w * 8 + 1 : (w - 64) * 8));
;                         attn_wg_task(F, l, task); }
.LBB0_521:
	v_readfirstlane_b32 s100, v212
	s_cmp_lt_u32 s100, 0x100
	s_cbranch_scc0 .Lattn_prio_0
	s_setprio 2
